# attention loop step 3: LDS-DMA issue block moved into the MFMA4-5 gap, accumulator init moved ahead of the barrier with v_mov_b64, six exp2 moved ahead of the first QK MFMA
# baseline (speedup 1.0000x reference)
; __device__ __forceinline__ unsigned pk4_fp8(float x0, float x1, float x2, float x3) { int w = 0; w = __builtin_amdgcn_cvt_pk_fp8_f32(x0, x1, w, false); w = __builtin_amdgcn_cvt_pk_fp8_f32(x2, x3, w, true); return (unsigned)w; }
; #define WAITBAR() do { asm volatile("s_waitcnt vmcnt(0)" ::: "memory"); __syncthreads(); } while (0)
; __device__ __forceinline__ void attn_unit(const bf16_t* Qb, const unsigned char* Kh, const unsigned char* Vh, bf16_t* Ob, int seq, int cbase, int lbase, int t0, const f32x2* atab, char* lds, const int wave_s) {
;     ...
; #pragma unroll
;     for (int ks = 0; ks < 3; ++ks) {
;         float x[32];
; #pragma unroll
;         for (int c4 = 0; c4 < 4; ++c4) { const u32x4 w = *reinterpret_cast<const u32x4*>(Qw + ks * 64 + c4 * 8);
;             x[8 * c4 + 0] = bflo(w.x); x[8 * c4 + 1] = bfhi(w.x); x[8 * c4 + 2] = bflo(w.y); x[8 * c4 + 3] = bfhi(w.y); x[8 * c4 + 4] = bflo(w.z); x[8 * c4 + 5] = bfhi(w.z); x[8 * c4 + 6] = bflo(w.w); x[8 * c4 + 7] = bfhi(w.w); }
;         if (ks == 2 && t0 >= 0) { const int t = t0 + wid * QBLK + r32; const int pos = hi ? (t & 63) : (t >> 6); const f32x2* tb = atab + pos * 16;
; #pragma unroll
;             for (int f = 0; f < 16; ++f) { const f32x2 cs = tb[f]; const float a = x[2 * f], b = x[2 * f + 1]; x[2 * f] = a * cs.x - b * cs.y; x[2 * f + 1] = b * cs.x + a * cs.y; } }
;         v8i q;
; #pragma unroll
;         for (int c = 0; c < 8; ++c) q[c] = (int)pk4_fp8(x[4 * c] * QC_Q, x[4 * c + 1] * QC_Q, x[4 * c + 2] * QC_Q, x[4 * c + 3] * QC_Q);
;         qr[ks] = q; }
;     ...
;     DMA_TILE(0, 0); DMA_TILE(1, 1); WAITBAR();
.LBB0_548:
	v_mul_f32_e32 v38, 0x3fd53b94, v54
	v_mul_f32_e32 v39, 0x3fd53b94, v46
	v_mov_b32_e32 v112, v153
	v_cvt_pk_fp8_f32 v112, v38, v39
	v_mul_f32_e32 v37, 0x3fd53b94, v37
	v_mul_f32_e32 v38, 0x3fd53b94, v63
	v_mov_b32_e32 v113, v153
	v_cvt_pk_fp8_f32 v113, v37, v38
	v_mul_f32_e32 v36, 0x3fd53b94, v36
	v_mul_f32_e32 v46, 0x3fd53b94, v62
	v_cvt_pk_fp8_f32 v112, v36, v46 op_sel:[0,0,1]
	v_mul_f32_e32 v35, 0x3fd53b94, v35
	v_mul_f32_e32 v36, 0x3fd53b94, v61
	v_cvt_pk_fp8_f32 v113, v35, v36 op_sel:[0,0,1]
	v_mul_f32_e32 v34, 0x3fd53b94, v34
	v_mul_f32_e32 v35, 0x3fd53b94, v60
	v_mov_b32_e32 v114, v153
	v_cvt_pk_fp8_f32 v114, v34, v35
	v_mul_f32_e32 v33, 0x3fd53b94, v33
	v_mul_f32_e32 v34, 0x3fd53b94, v59
	v_mov_b32_e32 v115, v153
	v_cvt_pk_fp8_f32 v115, v33, v34
	v_mul_f32_e32 v32, 0x3fd53b94, v32
	v_mul_f32_e32 v36, 0x3fd53b94, v58
	v_cvt_pk_fp8_f32 v114, v32, v36 op_sel:[0,0,1]
	v_mul_f32_e32 v32, 0x3fd53b94, v65
	v_mul_f32_e32 v33, 0x3fd53b94, v57
	v_cvt_pk_fp8_f32 v115, v32, v33 op_sel:[0,0,1]
	v_lshlrev_b32_e32 v32, 16, v28
	v_and_b32_e32 v28, 0xffff0000, v28
	v_lshlrev_b32_e32 v34, 16, v30
	v_and_b32_e32 v30, 0xffff0000, v30
	v_mul_f32_e32 v32, 0x3fd53b94, v32
	v_mul_f32_e32 v28, 0x3fd53b94, v28
	v_mov_b32_e32 v120, v153
	v_cvt_pk_fp8_f32 v120, v32, v28
	v_mul_f32_e32 v28, 0x3fd53b94, v34
	v_mul_f32_e32 v30, 0x3fd53b94, v30
	v_mov_b32_e32 v121, v153
	v_cvt_pk_fp8_f32 v121, v28, v30
	v_lshlrev_b32_e32 v33, 16, v29
	v_and_b32_e32 v29, 0xffff0000, v29
	v_lshlrev_b32_e32 v35, 16, v31
	v_and_b32_e32 v31, 0xffff0000, v31
	v_mul_f32_e32 v33, 0x3fd53b94, v33
	v_mul_f32_e32 v29, 0x3fd53b94, v29
	v_lshlrev_b32_e32 v36, 16, v24
	v_and_b32_e32 v24, 0xffff0000, v24
	v_cvt_pk_fp8_f32 v120, v33, v29 op_sel:[0,0,1]
	v_mul_f32_e32 v28, 0x3fd53b94, v35
	v_mul_f32_e32 v29, 0x3fd53b94, v31
	v_lshlrev_b32_e32 v38, 16, v26
	v_and_b32_e32 v26, 0xffff0000, v26
	v_cvt_pk_fp8_f32 v121, v28, v29 op_sel:[0,0,1]
	v_mul_f32_e32 v28, 0x3fd53b94, v36
	v_mul_f32_e32 v24, 0x3fd53b94, v24
	v_mov_b32_e32 v122, v153
	v_cvt_pk_fp8_f32 v122, v28, v24
	v_mul_f32_e32 v24, 0x3fd53b94, v38
	v_mul_f32_e32 v26, 0x3fd53b94, v26
	v_mov_b32_e32 v123, v153
	v_cvt_pk_fp8_f32 v123, v24, v26
	v_lshlrev_b32_e32 v37, 16, v25
	v_and_b32_e32 v25, 0xffff0000, v25
	v_lshlrev_b32_e32 v39, 16, v27
	v_and_b32_e32 v27, 0xffff0000, v27
	v_mul_f32_e32 v29, 0x3fd53b94, v37
	v_mul_f32_e32 v25, 0x3fd53b94, v25
	v_mul_f32_e32 v54, 0x3fd53b94, v56
	v_lshlrev_b32_e32 v56, 16, v20
	v_and_b32_e32 v20, 0xffff0000, v20
	v_cvt_pk_fp8_f32 v122, v29, v25 op_sel:[0,0,1]
	v_mul_f32_e32 v24, 0x3fd53b94, v39
	v_mul_f32_e32 v25, 0x3fd53b94, v27
	v_lshlrev_b32_e32 v58, 16, v22
	v_and_b32_e32 v22, 0xffff0000, v22
	v_cvt_pk_fp8_f32 v123, v24, v25 op_sel:[0,0,1]
	v_mul_f32_e32 v24, 0x3fd53b94, v56
	v_mul_f32_e32 v20, 0x3fd53b94, v20
	v_mov_b32_e32 v124, v153
	v_cvt_pk_fp8_f32 v124, v24, v20
	v_mul_f32_e32 v20, 0x3fd53b94, v58
	v_mul_f32_e32 v22, 0x3fd53b94, v22
	v_mov_b32_e32 v125, v153
	v_cvt_pk_fp8_f32 v125, v20, v22
	v_lshlrev_b32_e32 v57, 16, v21
	v_and_b32_e32 v21, 0xffff0000, v21
	v_lshlrev_b32_e32 v59, 16, v23
	v_and_b32_e32 v23, 0xffff0000, v23
	v_mul_f32_e32 v25, 0x3fd53b94, v57
	v_mul_f32_e32 v21, 0x3fd53b94, v21
	v_lshlrev_b32_e32 v60, 16, v16
	v_and_b32_e32 v16, 0xffff0000, v16
	v_cvt_pk_fp8_f32 v124, v25, v21 op_sel:[0,0,1]
	v_mul_f32_e32 v20, 0x3fd53b94, v59
	v_mul_f32_e32 v21, 0x3fd53b94, v23
	v_lshlrev_b32_e32 v62, 16, v18
	v_and_b32_e32 v18, 0xffff0000, v18
	v_cvt_pk_fp8_f32 v125, v20, v21 op_sel:[0,0,1]
	v_mul_f32_e32 v20, 0x3fd53b94, v60
	v_mul_f32_e32 v16, 0x3fd53b94, v16
	v_mov_b32_e32 v126, v153
	v_cvt_pk_fp8_f32 v126, v20, v16
	v_mul_f32_e32 v16, 0x3fd53b94, v62
	v_mul_f32_e32 v18, 0x3fd53b94, v18
	v_mov_b32_e32 v127, v153
	v_cvt_pk_fp8_f32 v127, v16, v18
	v_lshlrev_b32_e32 v61, 16, v17
	v_and_b32_e32 v17, 0xffff0000, v17
	v_lshlrev_b32_e32 v63, 16, v19
	v_and_b32_e32 v19, 0xffff0000, v19
	v_mul_f32_e32 v21, 0x3fd53b94, v61
	v_mul_f32_e32 v17, 0x3fd53b94, v17
	v_cvt_pk_fp8_f32 v126, v21, v17 op_sel:[0,0,1]
	v_mul_f32_e32 v16, 0x3fd53b94, v63
	v_mul_f32_e32 v17, 0x3fd53b94, v19
	v_cvt_pk_fp8_f32 v127, v16, v17 op_sel:[0,0,1]
	v_lshlrev_b32_e32 v16, 16, v12
	v_and_b32_e32 v12, 0xffff0000, v12
	v_lshlrev_b32_e32 v18, 16, v14
	v_and_b32_e32 v14, 0xffff0000, v14
	v_lshlrev_b32_e32 v58, 16, v0
	v_and_b32_e32 v59, 0xffff0000, v0
	v_lshlrev_b32_e32 v60, 16, v1
	v_and_b32_e32 v61, 0xffff0000, v1
	v_mul_f32_e32 v0, 0x3fd53b94, v16
	v_mul_f32_e32 v1, 0x3fd53b94, v12
	v_mov_b32_e32 v128, v153
	v_cvt_pk_fp8_f32 v128, v0, v1
	v_mul_f32_e32 v0, 0x3fd53b94, v18
	v_mul_f32_e32 v1, 0x3fd53b94, v14
	v_mov_b32_e32 v129, v153
	v_cvt_pk_fp8_f32 v129, v0, v1
	v_lshlrev_b32_e32 v19, 16, v15
	v_and_b32_e32 v15, 0xffff0000, v15
	v_lshlrev_b32_e32 v20, 16, v8
	v_and_b32_e32 v8, 0xffff0000, v8
	v_mul_f32_e32 v0, 0x3fd53b94, v19
	v_mul_f32_e32 v1, 0x3fd53b94, v15
	v_lshlrev_b32_e32 v22, 16, v10
	v_and_b32_e32 v10, 0xffff0000, v10
	v_cvt_pk_fp8_f32 v129, v0, v1 op_sel:[0,0,1]
	v_mul_f32_e32 v0, 0x3fd53b94, v20
	v_mul_f32_e32 v1, 0x3fd53b94, v8
	v_mov_b32_e32 v130, v153
	v_lshlrev_b32_e32 v17, 16, v13
	v_and_b32_e32 v13, 0xffff0000, v13
	v_cvt_pk_fp8_f32 v130, v0, v1
	v_mul_f32_e32 v0, 0x3fd53b94, v22
	v_mul_f32_e32 v1, 0x3fd53b94, v10
	v_mov_b32_e32 v131, v153
	v_mul_u32_u24_e32 v177, 0xd0, v155
	v_mul_f32_e32 v46, 0x3fd53b94, v64
	v_lshlrev_b32_e32 v21, 16, v9
	v_lshlrev_b32_e32 v23, 16, v11
	v_lshlrev_b32_e32 v62, 16, v2
	v_and_b32_e32 v63, 0xffff0000, v2
	v_lshlrev_b32_e32 v64, 16, v3
	v_and_b32_e32 v65, 0xffff0000, v3
	v_mul_f32_e32 v2, 0x3fd53b94, v17
	v_mul_f32_e32 v3, 0x3fd53b94, v13
	v_cvt_pk_fp8_f32 v131, v0, v1
	v_add3_u32 v178, 0, v177, v161
	v_cvt_pk_fp8_f32 v128, v2, v3 op_sel:[0,0,1]
	v_mul_f32_e32 v2, 0x3fd53b94, v21
	v_mul_f32_e32 v0, 0x3fd53b94, v23
	s_waitcnt vmcnt(0)
	s_waitcnt vmcnt(0) lgkmcnt(0)
	s_barrier
; __device__ __forceinline__ void qkt(f32x16& p0, f32x16& p1, const float m_reg, const char* Ks, const v8i* q8, int r32, int hi) {
;     { const float ini = PSH - m_reg;
; #pragma unroll
;       for (int r = 0; r < 16; ++r) { p0[r] = ini; p1[r] = ini; } }
; #pragma unroll
;     for (int ks = 0; ks < 3; ++ks) { const char* kp = Ks + r32 * KROWB + ks * 64 + hi * 32;
;         const v8i a0 = __builtin_shufflevector(*reinterpret_cast<const v4i*>(kp), *reinterpret_cast<const v4i*>(kp + 16), 0, 1, 2, 3, 4, 5, 6, 7);
;         const v8i a1 = __builtin_shufflevector(*reinterpret_cast<const v4i*>(kp + 32 * KROWB), *reinterpret_cast<const v4i*>(kp + 32 * KROWB + 16), 0, 1, 2, 3, 4, 5, 6, 7);
;         p0 = __builtin_amdgcn_mfma_scale_f32_32x32x64_f8f6f4(a0, q8[ks], p0, 0, 0, 0, QK_E, 0, QC_E);
;         p1 = __builtin_amdgcn_mfma_scale_f32_32x32x64_f8f6f4(a1, q8[ks], p1, 0, 0, 0, QK_E, 0, QC_E); }
; }
; __device__ __forceinline__ void attn_unit(const bf16_t* Qb, const unsigned char* Kh, const unsigned char* Vh, bf16_t* Ob, int seq, int cbase, int lbase, int t0, const f32x2* atab, char* lds, const int wave_s) {
;     ...
;     float m_reg = 0.f, l_reg = 0; f32x16 o[4] = {}; v8i qr[3];
;     const bf16_t* Qw = Qb + (long)(wid * QBLK + r32) * LDQ + hi * 32;
; #pragma unroll
;     for (int ks = 0; ks < 3; ++ks) {
;         float x[32];
; #pragma unroll
;         for (int c4 = 0; c4 < 4; ++c4) { const u32x4 w = *reinterpret_cast<const u32x4*>(Qw + ks * 64 + c4 * 8);
;             x[8 * c4 + 0] = bflo(w.x); x[8 * c4 + 1] = bfhi(w.x); x[8 * c4 + 2] = bflo(w.y); x[8 * c4 + 3] = bfhi(w.y); x[8 * c4 + 4] = bflo(w.z); x[8 * c4 + 5] = bfhi(w.z); x[8 * c4 + 6] = bflo(w.w); x[8 * c4 + 7] = bfhi(w.w); }
;         if (ks == 2 && t0 >= 0) { const int t = t0 + wid * QBLK + r32; const int pos = hi ? (t & 63) : (t >> 6); const f32x2* tb = atab + pos * 16;
; #pragma unroll
;             for (int f = 0; f < 16; ++f) { const f32x2 cs = tb[f]; const float a = x[2 * f], b = x[2 * f + 1]; x[2 * f] = a * cs.x - b * cs.y; x[2 * f + 1] = b * cs.x + a * cs.y; } }
;         v8i q;
; #pragma unroll
;         for (int c = 0; c < 8; ++c) q[c] = (int)pk4_fp8(x[4 * c] * QC_Q, x[4 * c + 1] * QC_Q, x[4 * c + 2] * QC_Q, x[4 * c + 3] * QC_Q);
;         qr[ks] = q; }
	ds_read_b128 v[16:19], v178
	ds_read_b128 v[20:23], v178 offset:16
	v_readlane_b32 s8, v254, 10
	v_and_b32_e32 v9, 0xffff0000, v9
	v_and_b32_e32 v11, 0xffff0000, v11
	v_readlane_b32 s9, v254, 11
	v_readlane_b32 s10, v254, 12
	v_readlane_b32 s11, v254, 13
	v_readlane_b32 s12, v254, 14
	v_readlane_b32 s13, v254, 15
	v_readlane_b32 s14, v254, 16
	v_readlane_b32 s15, v254, 17
	v_lshlrev_b32_e32 v24, 16, v4
	v_and_b32_e32 v4, 0xffff0000, v4
	v_lshlrev_b32_e32 v25, 16, v5
	v_and_b32_e32 v5, 0xffff0000, v5
	v_mul_f32_e32 v3, 0x3fd53b94, v9
	v_mul_f32_e32 v1, 0x3fd53b94, v11
	v_readlane_b32 s16, v254, 18
	v_readlane_b32 s17, v254, 19
	v_readlane_b32 s18, v254, 20
	v_readlane_b32 s19, v254, 21
	v_readlane_b32 s20, v254, 22
	v_readlane_b32 s21, v254, 23
	v_readlane_b32 s22, v254, 24
	v_readlane_b32 s23, v254, 25
	s_mov_b32 s9, s8
	s_mov_b32 s10, s8
	s_mov_b32 s11, s8
	s_mov_b32 s12, s8
	s_mov_b32 s13, s8
	s_mov_b32 s14, s8
	s_mov_b32 s15, s8
	s_mov_b32 s0, s8
	v_lshlrev_b32_e32 v32, 16, v6
	v_and_b32_e32 v33, 0xffff0000, v6
	v_lshlrev_b32_e32 v56, 16, v7
	v_and_b32_e32 v57, 0xffff0000, v7
	v_cvt_pk_fp8_f32 v130, v2, v3 op_sel:[0,0,1]
	v_cvt_pk_fp8_f32 v131, v0, v1 op_sel:[0,0,1]
	v_mul_f32_e32 v35, 0x3fd53b94, v4
	v_mul_f32_e32 v67, 0x3fd53b94, v5
	s_mov_b32 s16, s8
	s_mov_b32 s17, s8
	s_mov_b32 s18, s8
	s_mov_b32 s19, s8
	s_mov_b32 s20, s8
	s_mov_b32 s21, s8
	s_mov_b32 s22, s8
	s_mov_b32 s23, s8
	v_writelane_b32 v254, s0, 10
	v_mul_f32_e32 v34, 0x3fd53b94, v24
	v_mul_f32_e32 v66, 0x3fd53b94, v25
	v_mov_b64_e32 v[0:1], s[8:9]
	v_mov_b64_e32 v[2:3], s[10:11]
	v_mov_b64_e32 v[4:5], s[12:13]
	v_mov_b64_e32 v[6:7], s[14:15]
	v_mov_b64_e32 v[8:9], s[16:17]
	v_mov_b64_e32 v[10:11], s[18:19]
	v_mov_b64_e32 v[12:13], s[20:21]
	v_mov_b64_e32 v[14:15], s[22:23]
	v_mov_b32_e32 v132, v153
	v_mul_f32_e32 v32, 0x3fd53b94, v32
	s_waitcnt lgkmcnt(0)
	v_mfma_scale_f32_32x32x64_f8f6f4 v[16:31], v[16:23], v[120:127], v[0:15], v201, v200 op_sel_hi:[0,0,0]
	v_mul_f32_e32 v33, 0x3fd53b94, v33
	v_mov_b32_e32 v133, v153
	v_cvt_pk_fp8_f32 v132, v34, v35
	v_cvt_pk_fp8_f32 v133, v32, v33
	ds_read_b128 v[32:35], v178 offset:6656
	ds_read_b128 v[36:39], v178 offset:6672
	v_mul_f32_e32 v56, 0x3fd53b94, v56
	v_mul_f32_e32 v57, 0x3fd53b94, v57
	v_cvt_pk_fp8_f32 v133, v56, v57 op_sel:[0,0,1]
	v_mul_f32_e32 v56, 0x3fd53b94, v58
	v_mul_f32_e32 v57, 0x3fd53b94, v59
	v_mov_b32_e32 v134, v153
	v_cvt_pk_fp8_f32 v134, v56, v57
	v_mul_f32_e32 v56, 0x3fd53b94, v62
	v_mul_f32_e32 v57, 0x3fd53b94, v63
	v_mov_b32_e32 v135, v153
	s_waitcnt lgkmcnt(0)
	v_mfma_scale_f32_32x32x64_f8f6f4 v[0:15], v[32:39], v[120:127], v[0:15], v201, v200 op_sel_hi:[0,0,0]
	v_cvt_pk_fp8_f32 v135, v56, v57
	v_mul_f32_e32 v58, 0x3fd53b94, v60
	v_mul_f32_e32 v59, 0x3fd53b94, v61
	ds_read_b128 v[32:35], v178 offset:64
	ds_read_b128 v[36:39], v178 offset:80
	v_mul_f32_e32 v56, 0x3fd53b94, v64
	v_mul_f32_e32 v57, 0x3fd53b94, v65
	v_cvt_pk_fp8_f32 v132, v66, v67 op_sel:[0,0,1]
	v_cvt_pk_fp8_f32 v134, v58, v59 op_sel:[0,0,1]
	v_cvt_pk_fp8_f32 v135, v56, v57 op_sel:[0,0,1]
	v_mov_b32_e32 v117, v153
	v_mul_f32_e32 v41, 0x3fd53b94, v41
	v_mov_b32_e32 v118, v153
	v_mov_b32_e32 v116, v153
	v_mov_b32_e32 v119, v153
	v_cvt_pk_fp8_f32 v116, v46, v54
	s_waitcnt lgkmcnt(0)
	v_mfma_scale_f32_32x32x64_f8f6f4 v[16:31], v[32:39], v[128:135], v[16:31], v201, v200 op_sel_hi:[0,0,0]
	v_mul_f32_e32 v32, 0x3fd53b94, v52
	v_mul_f32_e32 v33, 0x3fd53b94, v40
	v_cvt_pk_fp8_f32 v117, v32, v33
	ds_read_b128 v[32:35], v178 offset:6720
	ds_read_b128 v[36:39], v178 offset:6736
	v_mul_f32_e32 v40, 0x3fd53b94, v53
	v_mul_f32_e32 v55, 0x3fd53b94, v55
	v_cvt_pk_fp8_f32 v117, v40, v41 op_sel:[0,0,1]
	v_mul_f32_e32 v40, 0x3fd53b94, v50
	v_mul_f32_e32 v41, 0x3fd53b94, v42
	v_cvt_pk_fp8_f32 v118, v40, v41
	v_mul_f32_e32 v40, 0x3fd53b94, v44
	v_mul_f32_e32 v41, 0x3fd53b94, v48
	v_cvt_pk_fp8_f32 v119, v40, v41
	v_mul_f32_e32 v47, 0x3fd53b94, v47
	v_mul_f32_e32 v42, 0x3fd53b94, v51
	s_waitcnt lgkmcnt(0)
	v_mfma_scale_f32_32x32x64_f8f6f4 v[0:15], v[32:39], v[128:135], v[0:15], v201, v200 op_sel_hi:[0,0,0]
	v_mul_f32_e32 v43, 0x3fd53b94, v43
	ds_read_b128 v[32:35], v178 offset:128
	ds_read_b128 v[36:39], v178 offset:144
	v_mul_f32_e32 v40, 0x3fd53b94, v45
	v_mul_f32_e32 v41, 0x3fd53b94, v49
	v_cvt_pk_fp8_f32 v116, v55, v47 op_sel:[0,0,1]
	v_cvt_pk_fp8_f32 v118, v42, v43 op_sel:[0,0,1]
	v_cvt_pk_fp8_f32 v119, v40, v41 op_sel:[0,0,1]
	v_writelane_b32 v254, s1, 11
	v_writelane_b32 v254, s2, 12
	v_writelane_b32 v254, s3, 13
	v_writelane_b32 v254, s4, 14
	v_writelane_b32 v254, s5, 15
	v_writelane_b32 v254, s6, 16
	v_writelane_b32 v254, s7, 17
	v_writelane_b32 v254, s8, 18
	s_waitcnt lgkmcnt(0)
	v_mfma_scale_f32_32x32x64_f8f6f4 v[16:31], v[32:39], v[112:119], v[16:31], v201, v200 op_sel_hi:[0,0,0]
	ds_read_b128 v[32:35], v178 offset:6784
	ds_read_b128 v[36:39], v178 offset:6800
	v_writelane_b32 v254, s9, 19
	v_writelane_b32 v254, s10, 20
	v_writelane_b32 v254, s11, 21
	v_writelane_b32 v254, s12, 22
	v_writelane_b32 v254, s13, 23
	v_writelane_b32 v254, s14, 24
	v_writelane_b32 v254, s15, 25
	v_readlane_b32 s0, v253, 34
	v_readlane_b32 s1, v253, 35
	s_ashr_i32 s1, s0, 31
	v_writelane_b32 v253, s0, 34
	s_add_i32 s7, s57, 0x80
	v_lshrrev_b32_e32 v172, 5, v72
	v_writelane_b32 v253, s1, 35
	s_waitcnt lgkmcnt(0)
; __device__ __forceinline__ float max3f(float a, float b, float c) { return fmaxf(fmaxf(a, b), c); }
; __device__ __forceinline__ void partialSM(f32x16& p0, f32x16& p1, float& m_reg, float& alpha, const bool first) {
;     float ma = max3f(p0[0], p0[1], p0[2]), mb = max3f(p0[3], p0[4], p0[5]), mc = max3f(p0[6], p0[7], p0[8]), md = max3f(p0[9], p0[10], p0[11]);
;     ma = max3f(ma, p0[12], p0[13]); mb = max3f(mb, p0[14], p0[15]); mc = max3f(mc, p1[0], p1[1]); md = max3f(md, p1[2], p1[3]);
;     ma = max3f(ma, p1[4], p1[5]); mb = max3f(mb, p1[6], p1[7]); mc = max3f(mc, p1[8], p1[9]); md = max3f(md, p1[10], p1[11]);
;     ma = max3f(ma, p1[12], p1[13]); mb = max3f(mb, p1[14], p1[15]);
;     float pmax = fmaxf(max3f(ma, mb, mc), md);
;     { auto rr = __builtin_amdgcn_permlane32_swap(__float_as_uint(pmax), __float_as_uint(pmax), false, false);
;       pmax = fmaxf(__uint_as_float(rr[0]), __uint_as_float(rr[1])); }
;     const float u = pmax - PSH;
;     if (__builtin_expect(!first && __all(u <= THR2), 1)) { alpha = 1.f; }
;     else { const float dl = first ? u : fmaxf(u, 0.f); alpha = __builtin_amdgcn_exp2f(-dl); m_reg += dl;
; #pragma unroll
;         for (int r = 0; r < 16; ++r) { p0[r] -= dl; p1[r] -= dl; } }
; #pragma unroll
;     for (int r = 0; r < 16; ++r) p0[r] = __builtin_amdgcn_exp2f(p0[r]);
; }
; __device__ __forceinline__ void qkt(f32x16& p0, f32x16& p1, const float m_reg, const char* Ks, const v8i* q8, int r32, int hi) {
;     { const float ini = PSH - m_reg;
; #pragma unroll
;       for (int r = 0; r < 16; ++r) { p0[r] = ini; p1[r] = ini; } }
	v_mfma_scale_f32_32x32x64_f8f6f4 v[0:15], v[32:39], v[112:119], v[0:15], v201, v200 op_sel_hi:[0,0,0]
	s_nop 1
	v_max_f32_e32 v32, v17, v17
	v_max_f32_e32 v33, v16, v16
	v_max_f32_e32 v32, v33, v32
	v_max3_f32 v33, v19, v20, v21
	v_max3_f32 v32, v32, v18, v28
	v_max3_f32 v33, v33, v30, v31
	v_max3_f32 v34, v22, v23, v24
	v_max3_f32 v35, v25, v26, v27
	v_readlane_b32 s1, v255, 19
	s_ashr_i32 s0, s1, 31
	s_lshr_b32 s0, s0, 26
	s_add_i32 s0, s1, s0
	s_ashr_i32 s6, s0, 6
	v_readlane_b32 s0, v255, 17
	s_lshl_b32 s2, s0, 13
	s_nop 2
	v_max3_f32 v32, v32, v29, v4
	v_max3_f32 v33, v33, v6, v7
	v_max3_f32 v34, v34, v0, v1
	v_max3_f32 v35, v35, v2, v3
	v_max3_f32 v32, v32, v5, v12
	v_max3_f32 v33, v33, v14, v15
	v_max3_f32 v34, v34, v8, v9
	v_max3_f32 v35, v35, v10, v11
	v_max3_f32 v32, v32, v13, v33
	v_max3_f32 v32, v32, v34, v35
	v_mov_b32_e32 v33, v32
	s_nop 1
	v_permlane32_swap_b32_e32 v32, v33
	v_max_f32_e32 v33, v33, v33
	v_max_f32_e32 v32, v32, v32
	v_max_f32_e32 v32, v32, v33
	v_add_f32_e32 v180, 0xc0400000, v32
	v_sub_f32_e32 v16, v16, v180
	v_exp_f32_e32 v215, v16
	v_sub_f32_e32 v16, v17, v180
	v_exp_f32_e32 v216, v16
	v_sub_f32_e32 v16, v18, v180
	v_exp_f32_e32 v190, v16
	v_sub_f32_e32 v16, v19, v180
	v_exp_f32_e32 v192, v16
	v_sub_f32_e32 v16, v20, v180
	v_exp_f32_e32 v213, v16
	v_sub_f32_e32 v16, v21, v180
	v_exp_f32_e32 v214, v16
	v_sub_f32_e32 v16, v22, v180
	v_exp_f32_e32 v195, v16
	v_sub_f32_e32 v16, v23, v180
	v_exp_f32_e32 v212, v16
	v_sub_f32_e32 v16, v24, v180
	v_exp_f32_e32 v194, v16
	v_sub_f32_e32 v16, v25, v180
	v_exp_f32_e32 v211, v16
	v_sub_f32_e32 v16, v26, v180
	v_exp_f32_e32 v186, v16
	v_sub_f32_e32 v16, v27, v180
	v_exp_f32_e32 v187, v16
	v_sub_f32_e32 v16, v28, v180
	v_exp_f32_e32 v191, v16
	v_sub_f32_e32 v16, v29, v180
	v_exp_f32_e32 v193, v16
	v_sub_f32_e32 v16, v30, v180
	v_readlane_b32 s0, v248, 27
	v_exp_f32_e32 v188, v16
	v_sub_f32_e32 v16, v31, v180
	v_sub_f32_e32 v64, v0, v180
	v_add_u32_e32 v0, s0, v80
	v_readlane_b32 s0, v252, 1
	v_exp_f32_e32 v189, v16
	v_exp_f32_e64 v181, -v180
	s_add_u32 s0, s0, s58
	v_readlane_b32 s1, v252, 2
	v_sub_f32_e32 v79, v15, v180
	v_sub_f32_e32 v78, v14, v180
	v_sub_f32_e32 v65, v1, v180
	v_mov_b32_e32 v1, v153
	s_addc_u32 s1, s1, s59
	v_mov_b32_e32 v14, v153
	v_mov_b32_e32 v15, v153
	v_sub_f32_e32 v77, v13, v180
	v_sub_f32_e32 v76, v12, v180
	v_sub_f32_e32 v75, v11, v180
	v_sub_f32_e32 v74, v10, v180
	v_sub_f32_e32 v73, v9, v180
	v_sub_f32_e32 v72, v8, v180
	v_sub_f32_e32 v71, v7, v180
	v_sub_f32_e32 v70, v6, v180
	v_sub_f32_e32 v69, v5, v180
	v_sub_f32_e32 v68, v4, v180
	v_sub_f32_e32 v67, v3, v180
	v_sub_f32_e32 v66, v2, v180
	v_lshl_add_u64 v[158:159], s[0:1], 0, v[0:1]
	v_mov_b32_e32 v0, v153
	v_mov_b32_e32 v2, v153
	v_mov_b32_e32 v3, v153
	v_mov_b32_e32 v4, v153
	v_mov_b32_e32 v5, v153
	v_mov_b32_e32 v6, v153
	v_mov_b32_e32 v7, v153
	v_mov_b32_e32 v8, v153
	v_mov_b32_e32 v9, v153
	v_mov_b32_e32 v10, v153
	v_mov_b32_e32 v11, v153
	v_mov_b32_e32 v12, v153
	v_mov_b32_e32 v13, v153
	v_mov_b64_e32 v[62:63], v[14:15]
	v_mov_b64_e32 v[46:47], v[14:15]
	v_mov_b64_e32 v[30:31], v[14:15]
	v_mul_u32_u24_e32 v179, 0x50, v155
	v_lshl_add_u32 v174, v155, 2, s31
	v_lshlrev_b32_e32 v173, 4, v172
	v_mov_b32_e32 v157, v153
	s_or_b32 s8, s2, 0x3c0
	s_mov_b32 s9, 0
	v_mov_b32_e32 v175, 0
	s_mov_b32 s11, 1
	v_mov_b64_e32 v[60:61], v[12:13]
	v_mov_b64_e32 v[58:59], v[10:11]
	v_mov_b64_e32 v[56:57], v[8:9]
	v_mov_b64_e32 v[54:55], v[6:7]
	v_mov_b64_e32 v[52:53], v[4:5]
	v_mov_b64_e32 v[50:51], v[2:3]
	v_mov_b64_e32 v[48:49], v[0:1]
	v_mov_b64_e32 v[44:45], v[12:13]
	v_mov_b64_e32 v[42:43], v[10:11]
	v_mov_b64_e32 v[40:41], v[8:9]
	v_mov_b64_e32 v[38:39], v[6:7]
	v_mov_b64_e32 v[36:37], v[4:5]
	v_mov_b64_e32 v[34:35], v[2:3]
	v_mov_b64_e32 v[32:33], v[0:1]
	v_mov_b64_e32 v[28:29], v[12:13]
	v_mov_b64_e32 v[26:27], v[10:11]
	v_mov_b64_e32 v[24:25], v[8:9]
	v_mov_b64_e32 v[22:23], v[6:7]
	v_mov_b64_e32 v[20:21], v[4:5]
	v_mov_b64_e32 v[18:19], v[2:3]
	v_mov_b64_e32 v[16:17], v[0:1]
	s_mov_b32 s13, 1
	s_mov_b32 s20, s3
	v_readlane_b32 s23, v255, 15
	v_sub_f32_e32 v80, 0x40400000, v180
	v_mov_b32_e32 v81, v80
	v_mov_b64_e32 v[82:83], v[80:81]
	v_mov_b64_e32 v[84:85], v[80:81]
	v_mov_b64_e32 v[86:87], v[80:81]
	v_mov_b64_e32 v[88:89], v[80:81]
	v_mov_b64_e32 v[90:91], v[80:81]
	v_mov_b64_e32 v[92:93], v[80:81]
	v_mov_b64_e32 v[94:95], v[80:81]
; __device__ __forceinline__ void finishSM(f32x16& p0, f32x16& p1, float alpha, float& l_reg, v8i& pa) {
; #pragma unroll
;     for (int r = 0; r < 16; ++r) p1[r] = __builtin_amdgcn_exp2f(p1[r]);
;     float sa = p0[0] + p0[1], sb = p0[2] + p0[3], sc = p0[4] + p0[5], sd = p0[6] + p0[7];
;     sa += p0[8]; sb += p0[9]; sc += p0[10]; sd += p0[11]; sa += p0[12]; sb += p0[13]; sc += p0[14]; sd += p0[15];
; #pragma unroll
;     for (int r = 0; r < 16; r += 4) { sa += p1[r]; sb += p1[r + 1]; sc += p1[r + 2]; sd += p1[r + 3]; }
;     float ps = (sa + sb) + (sc + sd);
;     { auto rr = __builtin_amdgcn_permlane32_swap(__float_as_uint(ps), __float_as_uint(ps), false, false);
;       ps = __uint_as_float(rr[0]) + __uint_as_float(rr[1]); }
;     l_reg = l_reg * alpha + ps;
; #pragma unroll
;     for (int c = 0; c < 4; ++c) { pa[c] = (int)pk4_fp8(p0[4 * c], p0[4 * c + 1], p0[4 * c + 2], p0[4 * c + 3]);
;         pa[4 + c] = (int)pk4_fp8(p1[4 * c], p1[4 * c + 1], p1[4 * c + 2], p1[4 * c + 3]); }
; }
; __device__ __forceinline__ void qkt(f32x16& p0, f32x16& p1, const float m_reg, const char* Ks, const v8i* q8, int r32, int hi) {
;     { const float ini = PSH - m_reg;
; #pragma unroll
;       for (int r = 0; r < 16; ++r) { p0[r] = ini; p1[r] = ini; } }
; #pragma unroll
;     for (int ks = 0; ks < 3; ++ks) { const char* kp = Ks + r32 * KROWB + ks * 64 + hi * 32;
;         const v8i a0 = __builtin_shufflevector(*reinterpret_cast<const v4i*>(kp), *reinterpret_cast<const v4i*>(kp + 16), 0, 1, 2, 3, 4, 5, 6, 7);
; __device__ __forceinline__ void attn_unit(const bf16_t* Qb, const unsigned char* Kh, const unsigned char* Vh, bf16_t* Ob, int seq, int cbase, int lbase, int t0, const f32x2* atab, char* lds, const int wave_s) {
;     ...
;     f32x16 pA0, pA1, pB0, pB1; float alA, alB; v8i pa; const int NT = seq / KVBLK;
;     DMA_TILE(0, 0); DMA_TILE(1, 1); WAITBAR();
;     qkt(pA0, pA1, m_reg, KBUF(0), qr, r32, hi); partialSM(pA0, pA1, m_reg, alA, true);
;     int bprev = 0, bj = 1;
;     for (int j = 1; j + 1 < NT; j += 2) {
;         { const int bn = 3 - bprev - bj; DMA_TILE(j + 1, bn);
;           SBAR(); qkt(pB0, pB1, m_reg, KBUF(bj), qr, r32, hi);
;           finishSM(pA0, pA1, alA, l_reg, pa); SBAR();
;           pv_d0(o, VBASE(bprev), pa, r32, hi); partialSM(pB0, pB1, m_reg, alB, false);
;           RESC(alB); WAITBAR(); bprev = bj; bj = bn; }
.LBB0_549:
	s_mul_i32 s0, s11, 0x5c00
	s_add_i32 s12, s0, 0
	v_add3_u32 v164, s12, v177, v161
	ds_read_b128 v[96:99], v164
	ds_read_b128 v[100:103], v164 offset:16
	ds_read_b128 v[136:139], v164 offset:6656
	ds_read_b128 v[140:143], v164 offset:6672
	v_exp_f32_e32 v228, v64
	v_exp_f32_e32 v230, v65
	v_exp_f32_e32 v222, v66
	v_exp_f32_e32 v223, v67
	v_exp_f32_e32 v229, v68
	v_exp_f32_e32 v231, v69
	v_exp_f32_e32 v226, v70
	v_exp_f32_e32 v227, v71
	s_waitcnt lgkmcnt(0)
	v_mfma_scale_f32_32x32x64_f8f6f4 v[96:111], v[96:103], v[120:127], v[80:95], v201, v200 op_sel_hi:[0,0,0]
	v_add_f32_e32 v64, v215, v216
	v_add_f32_e32 v65, v190, v192
	v_add_f32_e32 v66, v213, v214
	v_add_f32_e32 v67, v195, v212
	v_exp_f32_e32 v224, v72
	v_exp_f32_e32 v225, v73
	v_exp_f32_e32 v184, v74
	v_exp_f32_e32 v217, v75
	v_add_f32_e32 v64, v194, v64
	v_mfma_scale_f32_32x32x64_f8f6f4 v[80:95], v[136:143], v[120:127], v[80:95], v201, v200 op_sel_hi:[0,0,0]
	ds_read_b128 v[136:139], v164 offset:64
	ds_read_b128 v[140:143], v164 offset:80
	ds_read_b128 v[144:147], v164 offset:6720
	ds_read_b128 v[148:151], v164 offset:6736
	v_add_f32_e32 v65, v211, v65
	v_add_f32_e32 v66, v186, v66
	v_add_f32_e32 v67, v187, v67
	v_exp_f32_e32 v220, v76
	v_exp_f32_e32 v221, v77
	v_exp_f32_e32 v218, v78
	v_exp_f32_e32 v219, v79
	v_add_f32_e32 v64, v191, v64
	v_add_f32_e32 v65, v193, v65
	v_add_f32_e32 v66, v188, v66
	v_add_f32_e32 v67, v189, v67
	v_add_f32_e32 v64, v228, v64
	v_add_f32_e32 v65, v230, v65
	v_add_f32_e32 v66, v222, v66
	s_waitcnt lgkmcnt(0)
	v_mfma_scale_f32_32x32x64_f8f6f4 v[96:111], v[136:143], v[128:135], v[96:111], v201, v200 op_sel_hi:[0,0,0]
	v_add_f32_e32 v67, v223, v67
	v_add_f32_e32 v64, v229, v64
	v_add_f32_e32 v65, v231, v65
	v_add_f32_e32 v66, v226, v66
	v_add_f32_e32 v67, v227, v67
	v_add_f32_e32 v64, v224, v64
	v_add_f32_e32 v65, v225, v65
	v_add_f32_e32 v66, v184, v66
	v_add_f32_e32 v67, v217, v67
	v_add_f32_e32 v64, v220, v64
	v_add_f32_e32 v65, v221, v65
	v_add_f32_e32 v66, v218, v66
	v_add_f32_e32 v67, v219, v67
	v_add_f32_e32 v64, v65, v64
	v_add_f32_e32 v65, v66, v67
	v_mfma_scale_f32_32x32x64_f8f6f4 v[80:95], v[144:151], v[128:135], v[80:95], v201, v200 op_sel_hi:[0,0,0]
	ds_read_b128 v[136:139], v164 offset:128
	ds_read_b128 v[140:143], v164 offset:144
	ds_read_b128 v[144:147], v164 offset:6784
	ds_read_b128 v[148:151], v164 offset:6800
	s_add_i32 s0, s9, s11
	s_mov_b32 s10, s9
	s_sub_i32 s9, 3, s0
	s_sub_i32 s0, s8, 64
	s_cmp_lt_u32 s13, 3
	s_cselect_b32 s0, s7, s0
	s_mul_hi_i32 s1, s0, 0x300
	s_mulk_i32 s0, 0x300
	s_add_u32 s0, s55, s0
	s_mul_i32 s5, s9, 0x5c00
	s_addc_u32 s1, s56, s1
	s_add_i32 s2, s77, s5
	v_lshl_add_u64 v[166:167], s[0:1], 0, v[152:153]
	s_mov_b32 m0, s2
	s_and_b64 vcc, exec, s[46:47]
	global_load_lds_dwordx4 v[166:167], off
	s_cbranch_vccnz .LBB0_551
	v_lshl_add_u64 v[166:167], s[0:1], 0, v[156:157]
	s_add_i32 m0, s2, 0x2000
	s_nop 0
	global_load_lds_dwordx4 v[166:167], off

; __device__ __forceinline__ void partialSM(f32x16& p0, f32x16& p1, float& m_reg, float& alpha, const bool first) {
;     float ma = max3f(p0[0], p0[1], p0[2]), mb = max3f(p0[3], p0[4], p0[5]), mc = max3f(p0[6], p0[7], p0[8]), md = max3f(p0[9], p0[10], p0[11]);
;     ma = max3f(ma, p0[12], p0[13]); mb = max3f(mb, p0[14], p0[15]); mc = max3f(mc, p1[0], p1[1]); md = max3f(md, p1[2], p1[3]);
;     ma = max3f(ma, p1[4], p1[5]); mb = max3f(mb, p1[6], p1[7]); mc = max3f(mc, p1[8], p1[9]); md = max3f(md, p1[10], p1[11]);
;     ma = max3f(ma, p1[12], p1[13]); mb = max3f(mb, p1[14], p1[15]);
;     float pmax = fmaxf(max3f(ma, mb, mc), md);
;     { auto rr = __builtin_amdgcn_permlane32_swap(__float_as_uint(pmax), __float_as_uint(pmax), false, false);
;       pmax = fmaxf(__uint_as_float(rr[0]), __uint_as_float(rr[1])); }
;     const float u = pmax - PSH;
;     if (__builtin_expect(!first && __all(u <= THR2), 1)) { alpha = 1.f; }
;     else { const float dl = first ? u : fmaxf(u, 0.f); alpha = __builtin_amdgcn_exp2f(-dl); m_reg += dl;
; #pragma unroll
;         for (int r = 0; r < 16; ++r) { p0[r] -= dl; p1[r] -= dl; } }
; #pragma unroll
;     for (int r = 0; r < 16; ++r) p0[r] = __builtin_amdgcn_exp2f(p0[r]);
; }
; __device__ __forceinline__ void finishSM(f32x16& p0, f32x16& p1, float alpha, float& l_reg, v8i& pa) {
; #pragma unroll
;     for (int r = 0; r < 16; ++r) p1[r] = __builtin_amdgcn_exp2f(p1[r]);
;     float sa = p0[0] + p0[1], sb = p0[2] + p0[3], sc = p0[4] + p0[5], sd = p0[6] + p0[7];
;     sa += p0[8]; sb += p0[9]; sc += p0[10]; sd += p0[11]; sa += p0[12]; sb += p0[13]; sc += p0[14]; sd += p0[15];
; #pragma unroll
;     for (int r = 0; r < 16; r += 4) { sa += p1[r]; sb += p1[r + 1]; sc += p1[r + 2]; sd += p1[r + 3]; }
;     float ps = (sa + sb) + (sc + sd);
;     { auto rr = __builtin_amdgcn_permlane32_swap(__float_as_uint(ps), __float_as_uint(ps), false, false);
;       ps = __uint_as_float(rr[0]) + __uint_as_float(rr[1]); }
;     l_reg = l_reg * alpha + ps;
; #pragma unroll
;     for (int c = 0; c < 4; ++c) { pa[c] = (int)pk4_fp8(p0[4 * c], p0[4 * c + 1], p0[4 * c + 2], p0[4 * c + 3]);
;         pa[4 + c] = (int)pk4_fp8(p1[4 * c], p1[4 * c + 1], p1[4 * c + 2], p1[4 * c + 3]); }
; }
; __device__ __forceinline__ void qkt(f32x16& p0, f32x16& p1, const float m_reg, const char* Ks, const v8i* q8, int r32, int hi) {
;     { const float ini = PSH - m_reg;
.LBB0_553:
	v_add_f32_e32 v182, v65, v64
	v_mov_b32_e32 v183, v182
	v_cvt_pk_fp8_f32 v232, v215, v216
	v_cvt_pk_fp8_f32 v236, v228, v230
	v_cvt_pk_fp8_f32 v233, v213, v214
	v_cvt_pk_fp8_f32 v237, v229, v231
	v_cvt_pk_fp8_f32 v234, v194, v211
	v_cvt_pk_fp8_f32 v238, v224, v225
	v_cvt_pk_fp8_f32 v235, v191, v193
	v_cvt_pk_fp8_f32 v239, v220, v221
	v_permlane32_swap_b32_e32 v182, v183
	s_waitcnt lgkmcnt(0)
	v_mfma_scale_f32_32x32x64_f8f6f4 v[96:111], v[136:143], v[112:119], v[96:111], v201, v200 op_sel_hi:[0,0,0]
	v_cvt_pk_fp8_f32 v232, v190, v192 op_sel:[0,0,1]
	v_cvt_pk_fp8_f32 v236, v222, v223 op_sel:[0,0,1]
	v_cvt_pk_fp8_f32 v233, v195, v212 op_sel:[0,0,1]
	v_cvt_pk_fp8_f32 v237, v226, v227 op_sel:[0,0,1]
	v_cvt_pk_fp8_f32 v234, v186, v187 op_sel:[0,0,1]
	v_cvt_pk_fp8_f32 v238, v184, v217 op_sel:[0,0,1]
	v_cvt_pk_fp8_f32 v235, v188, v189 op_sel:[0,0,1]
	v_cvt_pk_fp8_f32 v239, v218, v219 op_sel:[0,0,1]
	v_mfma_scale_f32_32x32x64_f8f6f4 v[80:95], v[144:151], v[112:119], v[80:95], v201, v200 op_sel_hi:[0,0,0]
	s_mul_i32 s15, s10, 0x5c00
	s_add_i32 s11, s15, 0
	v_add_u32_e32 v64, s11, v161
	v_add_u32_e32 v176, v64, v179
	ds_read_b128 v[144:147], v176 offset:13312
	ds_read_b128 v[148:151], v176 offset:13328
	ds_read_b128 v[136:139], v176 offset:15872
	ds_read_b128 v[140:143], v176 offset:15888
	ds_read_b128 v[72:75], v176 offset:18432
	ds_read_b128 v[76:79], v176 offset:18448
	ds_read_b128 v[64:67], v176 offset:20992
	ds_read_b128 v[68:71], v176 offset:21008
	v_max_f32_e32 v164, v97, v97
	v_max_f32_e32 v165, v96, v96
	v_max_f32_e32 v164, v165, v164
	v_max3_f32 v165, v99, v100, v101
	v_max3_f32 v164, v164, v98, v108
	v_max3_f32 v165, v165, v110, v111
	v_max3_f32 v166, v102, v103, v104
	v_max3_f32 v167, v105, v106, v107
	s_waitcnt lgkmcnt(0)
	v_mfma_scale_f32_32x32x64_f8f6f4 v[0:15], v[232:239], v[144:151], v[0:15], v201, v201 op_sel_hi:[0,0,0]
	v_max3_f32 v164, v164, v109, v84
	v_max3_f32 v165, v165, v86, v87
	v_max3_f32 v166, v166, v80, v81
	v_max3_f32 v167, v167, v82, v83
	v_max3_f32 v164, v164, v85, v92
	v_max3_f32 v165, v165, v94, v95
	v_max3_f32 v166, v166, v88, v89
	v_max3_f32 v167, v167, v90, v91
	v_mfma_scale_f32_32x32x64_f8f6f4 v[48:63], v[232:239], v[136:143], v[48:63], v201, v201 op_sel_hi:[0,0,0]
	v_max3_f32 v164, v164, v93, v165
	v_max3_f32 v164, v164, v166, v167
	v_mov_b32_e32 v165, v164
	s_nop 1
	v_permlane32_swap_b32_e32 v164, v165
	v_max_f32_e32 v165, v165, v165
	v_max_f32_e32 v164, v164, v164
	v_max_f32_e32 v164, v164, v165
	v_add_f32_e32 v165, 0xc0400000, v164
	s_mov_b32 s0, 0x40b8aa3b
	v_cmp_ge_f32_e32 vcc, s0, v165
	s_cmp_eq_u64 vcc, exec
	v_mov_b32_e32 v185, 1.0
	s_cbranch_scc0 .LBB0_570

; #define SBAR() __builtin_amdgcn_sched_barrier(0)
; #define WAITBAR() do { asm volatile("s_waitcnt vmcnt(0)" ::: "memory"); __syncthreads(); } while (0)
; __device__ __forceinline__ void qkt(f32x16& p0, f32x16& p1, const float m_reg, const char* Ks, const v8i* q8, int r32, int hi) {
;     { const float ini = PSH - m_reg;
; #pragma unroll
;       for (int r = 0; r < 16; ++r) { p0[r] = ini; p1[r] = ini; } }
; #pragma unroll
;     for (int ks = 0; ks < 3; ++ks) { const char* kp = Ks + r32 * KROWB + ks * 64 + hi * 32;
;         const v8i a0 = __builtin_shufflevector(*reinterpret_cast<const v4i*>(kp), *reinterpret_cast<const v4i*>(kp + 16), 0, 1, 2, 3, 4, 5, 6, 7);
;         const v8i a1 = __builtin_shufflevector(*reinterpret_cast<const v4i*>(kp + 32 * KROWB), *reinterpret_cast<const v4i*>(kp + 32 * KROWB + 16), 0, 1, 2, 3, 4, 5, 6, 7);
;         p0 = __builtin_amdgcn_mfma_scale_f32_32x32x64_f8f6f4(a0, q8[ks], p0, 0, 0, 0, QK_E, 0, QC_E);
;         p1 = __builtin_amdgcn_mfma_scale_f32_32x32x64_f8f6f4(a1, q8[ks], p1, 0, 0, 0, QK_E, 0, QC_E); }
; }
; __device__ __forceinline__ void attn_unit(const bf16_t* Qb, const unsigned char* Kh, const unsigned char* Vh, bf16_t* Ob, int seq, int cbase, int lbase, int t0, const f32x2* atab, char* lds, const int wave_s) {
;     ...
;     f32x16 pA0, pA1, pB0, pB1; float alA, alB; v8i pa; const int NT = seq / KVBLK;
;     DMA_TILE(0, 0); DMA_TILE(1, 1); WAITBAR();
;     qkt(pA0, pA1, m_reg, KBUF(0), qr, r32, hi); partialSM(pA0, pA1, m_reg, alA, true);
;     int bprev = 0, bj = 1;
;     for (int j = 1; j + 1 < NT; j += 2) {
;         { const int bn = 3 - bprev - bj; DMA_TILE(j + 1, bn);
;           SBAR(); qkt(pB0, pB1, m_reg, KBUF(bj), qr, r32, hi);
;           finishSM(pA0, pA1, alA, l_reg, pa); SBAR();
;           pv_d0(o, VBASE(bprev), pa, r32, hi); partialSM(pB0, pB1, m_reg, alB, false);
;           RESC(alB); WAITBAR(); bprev = bj; bj = bn; }
;         { const int bn = 3 - bprev - bj; if (j + 2 < NT) DMA_TILE(j + 2, bn);
;           SBAR(); qkt(pA0, pA1, m_reg, KBUF(bj), qr, r32, hi);
;           finishSM(pB0, pB1, alB, l_reg, pa); SBAR();
;           pv_d0(o, VBASE(bprev), pa, r32, hi); partialSM(pA0, pA1, m_reg, alA, false);
;           RESC(alA); WAITBAR(); bprev = bj; bj = bn; }
.LBB0_558:
	v_sub_f32_e32 v64, 0x40400000, v180
	v_mov_b32_e32 v65, v64
	v_mov_b64_e32 v[66:67], v[64:65]
	v_mov_b64_e32 v[68:69], v[64:65]
	v_mov_b64_e32 v[70:71], v[64:65]
	v_mov_b64_e32 v[72:73], v[64:65]
	v_mov_b64_e32 v[74:75], v[64:65]
	v_mov_b64_e32 v[76:77], v[64:65]
	v_mov_b64_e32 v[78:79], v[64:65]
	s_waitcnt vmcnt(0)
	s_add_i32 s14, s13, 2
	s_cmp_ge_i32 s14, s6
	s_waitcnt vmcnt(0)
	s_barrier
	v_add_u32_e32 v164, s5, v178
	ds_read_b128 v[96:99], v164
	ds_read_b128 v[100:103], v164 offset:16
	ds_read_b128 v[136:139], v164 offset:6656
	ds_read_b128 v[140:143], v164 offset:6672
	v_exp_f32_e32 v231, v80
	v_exp_f32_e32 v233, v81
	v_exp_f32_e32 v225, v82
	v_exp_f32_e32 v226, v83
	v_exp_f32_e32 v232, v84
	v_exp_f32_e32 v234, v85
	v_exp_f32_e32 v229, v86
	v_exp_f32_e32 v230, v87
	s_waitcnt lgkmcnt(0)
	v_mfma_scale_f32_32x32x64_f8f6f4 v[96:111], v[96:103], v[120:127], v[64:79], v201, v200 op_sel_hi:[0,0,0]
	v_add_f32_e32 v80, v216, v215
	v_add_f32_e32 v81, v194, v192
	v_add_f32_e32 v82, v214, v213
	v_add_f32_e32 v83, v212, v211
	v_exp_f32_e32 v227, v88
	v_exp_f32_e32 v228, v89
	v_exp_f32_e32 v219, v90
	v_exp_f32_e32 v220, v91
	v_add_f32_e32 v80, v193, v80
	v_mfma_scale_f32_32x32x64_f8f6f4 v[64:79], v[136:143], v[120:127], v[64:79], v201, v200 op_sel_hi:[0,0,0]
	ds_read_b128 v[136:139], v164 offset:64
	ds_read_b128 v[140:143], v164 offset:80
	ds_read_b128 v[144:147], v164 offset:6720
	ds_read_b128 v[148:151], v164 offset:6736
	v_add_f32_e32 v81, v195, v81
	v_add_f32_e32 v82, v186, v82
	v_add_f32_e32 v83, v187, v83
	v_exp_f32_e32 v223, v92
	v_exp_f32_e32 v224, v93
	v_exp_f32_e32 v221, v94
	v_exp_f32_e32 v222, v95
	v_add_f32_e32 v80, v190, v80
	v_add_f32_e32 v81, v191, v81
	v_add_f32_e32 v82, v188, v82
	v_add_f32_e32 v83, v189, v83
	v_add_f32_e32 v80, v80, v231
	v_add_f32_e32 v81, v81, v233
	v_add_f32_e32 v82, v82, v225
	s_waitcnt lgkmcnt(0)
	v_mfma_scale_f32_32x32x64_f8f6f4 v[96:111], v[136:143], v[128:135], v[96:111], v201, v200 op_sel_hi:[0,0,0]
	v_add_f32_e32 v83, v83, v226
	v_add_f32_e32 v80, v232, v80
	v_add_f32_e32 v81, v234, v81
	v_add_f32_e32 v82, v229, v82
	v_add_f32_e32 v83, v230, v83
	v_add_f32_e32 v80, v227, v80
	v_add_f32_e32 v81, v228, v81
	v_add_f32_e32 v82, v219, v82
	v_add_f32_e32 v83, v220, v83
	v_add_f32_e32 v80, v223, v80
	v_add_f32_e32 v81, v224, v81
	v_add_f32_e32 v82, v221, v82
	v_add_f32_e32 v83, v222, v83
	v_add_f32_e32 v80, v81, v80
	v_add_f32_e32 v81, v82, v83
	v_mfma_scale_f32_32x32x64_f8f6f4 v[64:79], v[144:151], v[128:135], v[64:79], v201, v200 op_sel_hi:[0,0,0]
	ds_read_b128 v[136:139], v164 offset:128
	ds_read_b128 v[140:143], v164 offset:144
	ds_read_b128 v[144:147], v164 offset:6784
	ds_read_b128 v[148:151], v164 offset:6800
	s_cmp_ge_i32 s14, s6
	s_cbranch_scc1 .LBB0_563
	s_add_i32 s0, s7, 64
	s_cmp_lt_u32 s13, 2
	s_cselect_b32 s0, s0, s8
	s_mul_hi_i32 s1, s0, 0x300
	s_mulk_i32 s0, 0x300
	s_add_u32 s0, s55, s0
	s_addc_u32 s1, s56, s1
	s_add_i32 s13, s77, s15
	v_lshl_add_u64 v[166:167], s[0:1], 0, v[152:153]
	s_mov_b32 m0, s13
	s_and_b64 vcc, exec, s[46:47]
	global_load_lds_dwordx4 v[166:167], off
	s_cbranch_vccnz .LBB0_561
	v_lshl_add_u64 v[166:167], s[0:1], 0, v[156:157]
	s_add_i32 m0, s13, 0x2000
	s_nop 0
	global_load_lds_dwordx4 v[166:167], off

; __device__ __forceinline__ void partialSM(f32x16& p0, f32x16& p1, float& m_reg, float& alpha, const bool first) {
;     float ma = max3f(p0[0], p0[1], p0[2]), mb = max3f(p0[3], p0[4], p0[5]), mc = max3f(p0[6], p0[7], p0[8]), md = max3f(p0[9], p0[10], p0[11]);
;     ma = max3f(ma, p0[12], p0[13]); mb = max3f(mb, p0[14], p0[15]); mc = max3f(mc, p1[0], p1[1]); md = max3f(md, p1[2], p1[3]);
;     ma = max3f(ma, p1[4], p1[5]); mb = max3f(mb, p1[6], p1[7]); mc = max3f(mc, p1[8], p1[9]); md = max3f(md, p1[10], p1[11]);
;     ma = max3f(ma, p1[12], p1[13]); mb = max3f(mb, p1[14], p1[15]);
;     float pmax = fmaxf(max3f(ma, mb, mc), md);
;     { auto rr = __builtin_amdgcn_permlane32_swap(__float_as_uint(pmax), __float_as_uint(pmax), false, false);
;       pmax = fmaxf(__uint_as_float(rr[0]), __uint_as_float(rr[1])); }
;     const float u = pmax - PSH;
;     if (__builtin_expect(!first && __all(u <= THR2), 1)) { alpha = 1.f; }
;     else { const float dl = first ? u : fmaxf(u, 0.f); alpha = __builtin_amdgcn_exp2f(-dl); m_reg += dl;
; #pragma unroll
;         for (int r = 0; r < 16; ++r) { p0[r] -= dl; p1[r] -= dl; } }
; #pragma unroll
;     for (int r = 0; r < 16; ++r) p0[r] = __builtin_amdgcn_exp2f(p0[r]);
; }
; __device__ __forceinline__ void finishSM(f32x16& p0, f32x16& p1, float alpha, float& l_reg, v8i& pa) {
; #pragma unroll
;     for (int r = 0; r < 16; ++r) p1[r] = __builtin_amdgcn_exp2f(p1[r]);
;     float sa = p0[0] + p0[1], sb = p0[2] + p0[3], sc = p0[4] + p0[5], sd = p0[6] + p0[7];
;     sa += p0[8]; sb += p0[9]; sc += p0[10]; sd += p0[11]; sa += p0[12]; sb += p0[13]; sc += p0[14]; sd += p0[15];
; #pragma unroll
;     for (int r = 0; r < 16; r += 4) { sa += p1[r]; sb += p1[r + 1]; sc += p1[r + 2]; sd += p1[r + 3]; }
;     float ps = (sa + sb) + (sc + sd);
;     { auto rr = __builtin_amdgcn_permlane32_swap(__float_as_uint(ps), __float_as_uint(ps), false, false);
;       ps = __uint_as_float(rr[0]) + __uint_as_float(rr[1]); }
;     l_reg = l_reg * alpha + ps;
; #pragma unroll
;     for (int c = 0; c < 4; ++c) { pa[c] = (int)pk4_fp8(p0[4 * c], p0[4 * c + 1], p0[4 * c + 2], p0[4 * c + 3]);
;         pa[4 + c] = (int)pk4_fp8(p1[4 * c], p1[4 * c + 1], p1[4 * c + 2], p1[4 * c + 3]); }
; }
; __device__ __forceinline__ void qkt(f32x16& p0, f32x16& p1, const float m_reg, const char* Ks, const v8i* q8, int r32, int hi) {
;     { const float ini = PSH - m_reg;
.LBB0_563:
	v_add_f32_e32 v217, v81, v80
	v_mov_b32_e32 v218, v217
	v_cvt_pk_fp8_f32 v236, v215, v216
	v_cvt_pk_fp8_f32 v240, v231, v233
	v_cvt_pk_fp8_f32 v237, v213, v214
	v_cvt_pk_fp8_f32 v241, v232, v234
	v_cvt_pk_fp8_f32 v238, v193, v195
	v_cvt_pk_fp8_f32 v242, v227, v228
	v_cvt_pk_fp8_f32 v239, v190, v191
	v_cvt_pk_fp8_f32 v243, v223, v224
	v_permlane32_swap_b32_e32 v217, v218
	s_waitcnt lgkmcnt(0)
	v_mfma_scale_f32_32x32x64_f8f6f4 v[96:111], v[136:143], v[112:119], v[96:111], v201, v200 op_sel_hi:[0,0,0]
	v_cvt_pk_fp8_f32 v236, v192, v194 op_sel:[0,0,1]
	v_cvt_pk_fp8_f32 v240, v225, v226 op_sel:[0,0,1]
	v_cvt_pk_fp8_f32 v237, v211, v212 op_sel:[0,0,1]
	v_cvt_pk_fp8_f32 v241, v229, v230 op_sel:[0,0,1]
	v_cvt_pk_fp8_f32 v238, v186, v187 op_sel:[0,0,1]
	v_cvt_pk_fp8_f32 v242, v219, v220 op_sel:[0,0,1]
	v_cvt_pk_fp8_f32 v239, v188, v189 op_sel:[0,0,1]
	v_cvt_pk_fp8_f32 v243, v221, v222 op_sel:[0,0,1]
	v_mfma_scale_f32_32x32x64_f8f6f4 v[64:79], v[144:151], v[112:119], v[64:79], v201, v200 op_sel_hi:[0,0,0]
	v_add3_u32 v84, s12, v161, v179
	ds_read_b128 v[144:147], v84 offset:13312
	ds_read_b128 v[148:151], v84 offset:13328
	ds_read_b128 v[136:139], v84 offset:15872
	ds_read_b128 v[140:143], v84 offset:15888
	ds_read_b128 v[88:91], v84 offset:18432
	ds_read_b128 v[92:95], v84 offset:18448
	ds_read_b128 v[80:83], v84 offset:20992
	ds_read_b128 v[84:87], v84 offset:21008
	s_nop 1
	v_max_f32_e32 v164, v97, v97
	v_max_f32_e32 v165, v96, v96
	v_max_f32_e32 v164, v165, v164
	v_max3_f32 v165, v99, v100, v101
	v_max3_f32 v164, v164, v98, v108
	v_max3_f32 v165, v165, v110, v111
	v_max3_f32 v166, v102, v103, v104
	v_max3_f32 v167, v105, v106, v107
	s_waitcnt lgkmcnt(0)
	v_mfma_scale_f32_32x32x64_f8f6f4 v[0:15], v[236:243], v[144:151], v[0:15], v201, v201 op_sel_hi:[0,0,0]
	v_max3_f32 v164, v164, v109, v68
	v_max3_f32 v165, v165, v70, v71
	v_max3_f32 v166, v166, v64, v65
	v_max3_f32 v167, v167, v66, v67
	v_max3_f32 v164, v164, v69, v76
	v_max3_f32 v165, v165, v78, v79
	v_max3_f32 v166, v166, v72, v73
	v_max3_f32 v167, v167, v74, v75
	v_mfma_scale_f32_32x32x64_f8f6f4 v[48:63], v[236:243], v[136:143], v[48:63], v201, v201 op_sel_hi:[0,0,0]
	v_max3_f32 v164, v164, v77, v165
	v_max3_f32 v164, v164, v166, v167
	v_mov_b32_e32 v165, v164
	s_nop 1
	v_permlane32_swap_b32_e32 v164, v165
	v_max_f32_e32 v165, v165, v165
	v_max_f32_e32 v164, v164, v164
	v_max_f32_e32 v164, v164, v165
	v_add_f32_e32 v165, 0xc0400000, v164
	s_mov_b32 s0, 0x40b8aa3b
	v_cmp_ge_f32_e32 vcc, s0, v165
	s_cmp_eq_u64 vcc, exec
	v_mov_b32_e32 v184, 1.0
	s_cbranch_scc0 .LBB0_571

; #define SBAR() __builtin_amdgcn_sched_barrier(0)
; #define WAITBAR() do { asm volatile("s_waitcnt vmcnt(0)" ::: "memory"); __syncthreads(); } while (0)
; #define RESC(a) do { if (__any((a) < 1.f)) { if (hi == 0) al_l[r32] = (a); asm volatile("s_waitcnt lgkmcnt(0)" ::: "memory"); \
;     _Pragma("unroll") for (int d = 0; d < 4; ++d) _Pragma("unroll") for (int r = 0; r < 16; ++r) o[d][r] *= al_l[crow(r, hi)]; } } while (0)
; __device__ __forceinline__ void finishSM(f32x16& p0, f32x16& p1, float alpha, float& l_reg, v8i& pa) {
;     ...
;     l_reg = l_reg * alpha + ps;
; __device__ __forceinline__ void attn_unit(const bf16_t* Qb, const unsigned char* Kh, const unsigned char* Vh, bf16_t* Ob, int seq, int cbase, int lbase, int t0, const f32x2* atab, char* lds, const int wave_s) {
;     ...
;     for (int j = 1; j + 1 < NT; j += 2) {
;         { const int bn = 3 - bprev - bj; DMA_TILE(j + 1, bn);
;           SBAR(); qkt(pB0, pB1, m_reg, KBUF(bj), qr, r32, hi);
;           finishSM(pA0, pA1, alA, l_reg, pa); SBAR();
;           pv_d0(o, VBASE(bprev), pa, r32, hi); partialSM(pB0, pB1, m_reg, alB, false);
;           RESC(alB); WAITBAR(); bprev = bj; bj = bn; }
;         { const int bn = 3 - bprev - bj; if (j + 2 < NT) DMA_TILE(j + 2, bn);
;           SBAR(); qkt(pA0, pA1, m_reg, KBUF(bj), qr, r32, hi);
;           finishSM(pB0, pB1, alB, l_reg, pa); SBAR();
;           pv_d0(o, VBASE(bprev), pa, r32, hi); partialSM(pA0, pA1, m_reg, alA, false);
;           RESC(alA); WAITBAR(); bprev = bj; bj = bn; }
;     }
.LBB0_568:
	v_add_f32_e32 v80, v182, v183
	s_waitcnt vmcnt(0)
	s_addk_i32 s7, 0x80
	s_add_i32 s0, s14, 1
	s_addk_i32 s8, 0x80
	v_fmac_f32_e32 v80, v181, v175
	v_add_f32_e32 v175, v217, v218
	s_cmp_ge_i32 s0, s6
	s_mov_b64 s[0:1], 0x5000
	v_fmac_f32_e32 v175, v80, v185
	v_lshl_add_u64 v[158:159], v[158:159], 0, s[0:1]
	v_sub_f32_e32 v80, 0x40400000, v180
	v_mov_b32_e32 v81, v80
	v_mov_b64_e32 v[82:83], v[80:81]
	v_mov_b64_e32 v[84:85], v[80:81]
	v_mov_b64_e32 v[86:87], v[80:81]
	v_mov_b64_e32 v[88:89], v[80:81]
	v_mov_b64_e32 v[90:91], v[80:81]
	v_mov_b64_e32 v[92:93], v[80:81]
	v_mov_b64_e32 v[94:95], v[80:81]
	s_waitcnt vmcnt(0)
	s_barrier
	s_cbranch_scc1 .LBB0_572
	s_mov_b32 s11, s10
	s_mov_b32 s13, s14
	v_mov_b32_e32 v181, v184
	s_branch .LBB0_549
